# GEMM loops: removed the insurance s_nop pad in front of fp8 MFMA blocks whose operands come from waited LDS reads (no VALU producer nearby); on top of v69
# baseline (speedup 1.0000x reference)
.LBB0_182:
	ds_read_b128 v[16:19], v199
	ds_read_b128 v[20:23], v199 offset:1024
	ds_read_b128 v[24:27], v199 offset:2048
	ds_read_b128 v[28:31], v199 offset:3072
	ds_read_b128 v[0:3], v200
	ds_read_b128 v[4:7], v200 offset:1024
	ds_read_b128 v[8:11], v200 offset:2048
	ds_read_b128 v[12:15], v200 offset:3072
	s_add_u32 s6, s28, 0x100
	s_addc_u32 s7, s29, 0
	s_add_u32 s31, s21, s28
	s_addc_u32 s34, s25, s29
	s_cmpk_eq_i32 s28, 0x700
	s_cselect_b64 vcc, -1, 0
	s_and_b64 s[26:27], vcc, exec
	v_cndmask_b32_e32 v164, v206, v202, vcc
	s_cselect_b32 s27, s23, s34
	s_cselect_b32 s26, s22, s31
	v_cndmask_b32_e32 v188, v174, v203, vcc
	v_cndmask_b32_e32 v177, v176, v204, vcc
	v_cndmask_b32_e32 v179, v178, v205, vcc
	s_cselect_b32 s31, 0, s7
	s_cselect_b32 s34, 0, s6
	v_lshl_add_u64 v[184:185], v[182:183], 0, s[28:29]
	s_add_i32 m0, s3, 0xc000
	ds_read_b128 v[208:211], v201
	ds_read_b128 v[212:215], v201 offset:1024
	ds_read_b128 v[216:219], v201 offset:2048
	ds_read_b128 v[220:223], v201 offset:3072
	ds_read_b128 v[224:227], v201 offset:4096
	ds_read_b128 v[228:231], v201 offset:5120
	ds_read_b128 v[232:235], v201 offset:6144
	ds_read_b128 v[236:239], v201 offset:7168
	global_load_lds_dwordx4 v[184:185], off
	v_lshl_add_u64 v[184:185], v[180:181], 0, s[28:29]
	s_add_i32 m0, s3, 0xe000
	s_nop 0
	global_load_lds_dwordx4 v[184:185], off
	s_waitcnt vmcnt(8)
	s_waitcnt lgkmcnt(0)
	s_barrier
	s_setprio 1
	s_nop 1
	s_waitcnt lgkmcnt(0)
	v_mfma_scale_f32_16x16x128_f8f6f4 v[156:159], v[16:23], v[208:215], v[156:159], v197, v196 op_sel_hi:[0,0,0]
	v_mfma_scale_f32_16x16x128_f8f6f4 v[152:155], v[24:31], v[208:215], v[152:155], v197, v196 op_sel_hi:[0,0,0]
	v_mfma_scale_f32_16x16x128_f8f6f4 v[136:139], v[24:31], v[216:223], v[136:139], v197, v196 op_sel_hi:[0,0,0]
	v_mfma_scale_f32_16x16x128_f8f6f4 v[140:143], v[16:23], v[216:223], v[140:143], v197, v196 op_sel_hi:[0,0,0]
	v_mfma_scale_f32_16x16x128_f8f6f4 v[124:127], v[16:23], v[224:231], v[124:127], v197, v196 op_sel_hi:[0,0,0]
	v_mfma_scale_f32_16x16x128_f8f6f4 v[120:123], v[24:31], v[224:231], v[120:123], v197, v196 op_sel_hi:[0,0,0]
	v_mfma_scale_f32_16x16x128_f8f6f4 v[104:107], v[24:31], v[232:239], v[104:107], v197, v196 op_sel_hi:[0,0,0]
	v_mfma_scale_f32_16x16x128_f8f6f4 v[108:111], v[16:23], v[232:239], v[108:111], v197, v196 op_sel_hi:[0,0,0]
	s_setprio 0
	s_setprio 1
	v_mfma_scale_f32_16x16x128_f8f6f4 v[100:103], v[0:7], v[232:239], v[100:103], v197, v196 op_sel_hi:[0,0,0]
	v_mfma_scale_f32_16x16x128_f8f6f4 v[96:99], v[8:15], v[232:239], v[96:99], v197, v196 op_sel_hi:[0,0,0]
	v_mfma_scale_f32_16x16x128_f8f6f4 v[112:115], v[8:15], v[224:231], v[112:115], v197, v196 op_sel_hi:[0,0,0]
	v_mfma_scale_f32_16x16x128_f8f6f4 v[116:119], v[0:7], v[224:231], v[116:119], v197, v196 op_sel_hi:[0,0,0]
	v_mfma_scale_f32_16x16x128_f8f6f4 v[132:135], v[0:7], v[216:223], v[132:135], v197, v196 op_sel_hi:[0,0,0]
	v_mfma_scale_f32_16x16x128_f8f6f4 v[128:131], v[8:15], v[216:223], v[128:131], v197, v196 op_sel_hi:[0,0,0]
	v_mfma_scale_f32_16x16x128_f8f6f4 v[144:147], v[8:15], v[208:215], v[144:147], v197, v196 op_sel_hi:[0,0,0]
	v_mfma_scale_f32_16x16x128_f8f6f4 v[148:151], v[0:7], v[208:215], v[148:151], v197, v196 op_sel_hi:[0,0,0]
	s_setprio 0
	s_barrier
	s_add_i32 s28, s46, s2
	v_lshl_add_u64 v[184:185], s[26:27], 0, v[160:161]
	s_mov_b32 m0, s28
	ds_read_b128 v[208:211], v201 offset:16384
	ds_read_b128 v[212:215], v201 offset:17408
	ds_read_b128 v[216:219], v201 offset:18432
	ds_read_b128 v[220:223], v201 offset:19456
	ds_read_b128 v[224:227], v201 offset:20480
	ds_read_b128 v[228:231], v201 offset:21504
	ds_read_b128 v[232:235], v201 offset:22528
	ds_read_b128 v[236:239], v201 offset:23552
	global_load_lds_dwordx4 v[184:185], off
	s_add_i32 m0, s28, 0x2000
	s_add_u32 s28, s26, 0x4000
	v_lshl_add_u64 v[186:187], s[26:27], 0, v[162:163]
	s_addc_u32 s29, s27, 0
	s_add_i32 s35, s47, s2
	global_load_lds_dwordx4 v[186:187], off
	v_lshl_add_u64 v[190:191], s[28:29], 0, v[160:161]
	s_mov_b32 m0, s35
	v_mov_b32_e32 v189, v165
	global_load_lds_dwordx4 v[190:191], off
	s_add_i32 m0, s35, 0x2000
	v_lshl_add_u64 v[190:191], s[28:29], 0, v[162:163]
	s_add_u32 s28, s8, s34
	global_load_lds_dwordx4 v[190:191], off
	s_addc_u32 s29, s9, s31
	s_mov_b32 m0, s3
	v_lshl_add_u64 v[190:191], s[28:29], 0, v[164:165]
	global_load_lds_dwordx4 v164, s[28:29]
	s_mov_b32 m0, s33
	s_nop 0
	global_load_lds_dwordx4 v188, s[28:29]
	s_waitcnt vmcnt(8)
	s_waitcnt lgkmcnt(0)
	v_lshl_add_u64 v[188:189], s[28:29], 0, v[188:189]
	s_barrier
	s_setprio 1
	s_nop 1
	s_waitcnt lgkmcnt(0)
	v_mfma_scale_f32_16x16x128_f8f6f4 v[92:95], v[16:23], v[208:215], v[92:95], v197, v196 op_sel_hi:[0,0,0]
	v_mfma_scale_f32_16x16x128_f8f6f4 v[88:91], v[24:31], v[208:215], v[88:91], v197, v196 op_sel_hi:[0,0,0]
	v_mfma_scale_f32_16x16x128_f8f6f4 v[64:67], v[24:31], v[216:223], v[64:67], v197, v196 op_sel_hi:[0,0,0]
	v_mfma_scale_f32_16x16x128_f8f6f4 v[68:71], v[16:23], v[216:223], v[68:71], v197, v196 op_sel_hi:[0,0,0]
	v_mfma_scale_f32_16x16x128_f8f6f4 v[44:47], v[16:23], v[224:231], v[44:47], v197, v196 op_sel_hi:[0,0,0]
	v_mfma_scale_f32_16x16x128_f8f6f4 v[40:43], v[24:31], v[224:231], v[40:43], v197, v196 op_sel_hi:[0,0,0]
	v_mfma_scale_f32_16x16x128_f8f6f4 v[32:35], v[24:31], v[232:239], v[32:35], v197, v196 op_sel_hi:[0,0,0]
	v_mfma_scale_f32_16x16x128_f8f6f4 v[36:39], v[16:23], v[232:239], v[36:39], v197, v196 op_sel_hi:[0,0,0]
	s_setprio 0
	s_setprio 1
	v_mfma_scale_f32_16x16x128_f8f6f4 v[56:59], v[0:7], v[232:239], v[56:59], v197, v196 op_sel_hi:[0,0,0]
	v_mfma_scale_f32_16x16x128_f8f6f4 v[60:63], v[8:15], v[232:239], v[60:63], v197, v196 op_sel_hi:[0,0,0]
	v_mfma_scale_f32_16x16x128_f8f6f4 v[76:79], v[8:15], v[224:231], v[76:79], v197, v196 op_sel_hi:[0,0,0]
	v_mfma_scale_f32_16x16x128_f8f6f4 v[72:75], v[0:7], v[224:231], v[72:75], v197, v196 op_sel_hi:[0,0,0]
	v_mfma_scale_f32_16x16x128_f8f6f4 v[52:55], v[0:7], v[216:223], v[52:55], v197, v196 op_sel_hi:[0,0,0]
	v_mfma_scale_f32_16x16x128_f8f6f4 v[48:51], v[8:15], v[216:223], v[48:51], v197, v196 op_sel_hi:[0,0,0]
	v_mfma_scale_f32_16x16x128_f8f6f4 v[80:83], v[8:15], v[208:215], v[80:83], v197, v196 op_sel_hi:[0,0,0]
	v_mfma_scale_f32_16x16x128_f8f6f4 v[84:87], v[0:7], v[208:215], v[84:87], v197, v196 op_sel_hi:[0,0,0]
	s_setprio 0
	s_barrier
	s_add_i32 s31, 0, 0x18000
	s_add_i32 s34, 0, 0x1c000
	v_add_u32_e32 v12, s31, v198
	v_add_u32_e32 v28, s34, v198
	ds_read_b128 v[0:3], v12
	ds_read_b128 v[4:7], v12 offset:1024
	ds_read_b128 v[8:11], v12 offset:2048
	ds_read_b128 v[12:15], v12 offset:3072
	ds_read_b128 v[16:19], v28
	ds_read_b128 v[20:23], v28 offset:1024
	ds_read_b128 v[24:27], v28 offset:2048
	ds_read_b128 v[28:31], v28 offset:3072
	s_mov_b32 m0, s36
	ds_read_b128 v[208:211], v201 offset:32768
	ds_read_b128 v[212:215], v201 offset:33792
	ds_read_b128 v[216:219], v201 offset:34816
	ds_read_b128 v[220:223], v201 offset:35840
	ds_read_b128 v[224:227], v201 offset:36864
	ds_read_b128 v[228:231], v201 offset:37888
	ds_read_b128 v[232:235], v201 offset:38912
	ds_read_b128 v[236:239], v201 offset:39936
	global_load_lds_dwordx4 v177, s[28:29]
	s_mov_b32 m0, s37
	s_nop 0
	global_load_lds_dwordx4 v179, s[28:29]
	s_waitcnt vmcnt(8)
	s_waitcnt lgkmcnt(0)
	s_barrier
	s_setprio 1
	s_nop 1
	s_waitcnt lgkmcnt(0)
	v_mfma_scale_f32_16x16x128_f8f6f4 v[156:159], v[0:7], v[208:215], v[156:159], v197, v196 op_sel_hi:[0,0,0]
	v_mfma_scale_f32_16x16x128_f8f6f4 v[152:155], v[8:15], v[208:215], v[152:155], v197, v196 op_sel_hi:[0,0,0]
	v_mfma_scale_f32_16x16x128_f8f6f4 v[136:139], v[8:15], v[216:223], v[136:139], v197, v196 op_sel_hi:[0,0,0]
	v_mfma_scale_f32_16x16x128_f8f6f4 v[140:143], v[0:7], v[216:223], v[140:143], v197, v196 op_sel_hi:[0,0,0]
	v_mfma_scale_f32_16x16x128_f8f6f4 v[124:127], v[0:7], v[224:231], v[124:127], v197, v196 op_sel_hi:[0,0,0]
	v_mfma_scale_f32_16x16x128_f8f6f4 v[120:123], v[8:15], v[224:231], v[120:123], v197, v196 op_sel_hi:[0,0,0]
	v_mfma_scale_f32_16x16x128_f8f6f4 v[104:107], v[8:15], v[232:239], v[104:107], v197, v196 op_sel_hi:[0,0,0]
	v_mfma_scale_f32_16x16x128_f8f6f4 v[108:111], v[0:7], v[232:239], v[108:111], v197, v196 op_sel_hi:[0,0,0]
	s_setprio 0
	s_setprio 1
	v_mfma_scale_f32_16x16x128_f8f6f4 v[100:103], v[16:23], v[232:239], v[100:103], v197, v196 op_sel_hi:[0,0,0]
	v_mfma_scale_f32_16x16x128_f8f6f4 v[96:99], v[24:31], v[232:239], v[96:99], v197, v196 op_sel_hi:[0,0,0]
	v_mfma_scale_f32_16x16x128_f8f6f4 v[112:115], v[24:31], v[224:231], v[112:115], v197, v196 op_sel_hi:[0,0,0]
	v_mfma_scale_f32_16x16x128_f8f6f4 v[116:119], v[16:23], v[224:231], v[116:119], v197, v196 op_sel_hi:[0,0,0]
	v_mfma_scale_f32_16x16x128_f8f6f4 v[132:135], v[16:23], v[216:223], v[132:135], v197, v196 op_sel_hi:[0,0,0]
	v_mfma_scale_f32_16x16x128_f8f6f4 v[128:131], v[24:31], v[216:223], v[128:131], v197, v196 op_sel_hi:[0,0,0]
	v_mfma_scale_f32_16x16x128_f8f6f4 v[144:147], v[24:31], v[208:215], v[144:147], v197, v196 op_sel_hi:[0,0,0]
	v_mfma_scale_f32_16x16x128_f8f6f4 v[148:151], v[16:23], v[208:215], v[148:151], v197, v196 op_sel_hi:[0,0,0]
	s_setprio 0
	s_barrier
	s_add_i32 s28, s31, s2
	v_lshl_add_u64 v[184:185], v[184:185], 0, s[12:13]
	s_mov_b32 m0, s28
	ds_read_b128 v[208:211], v201 offset:49152
	ds_read_b128 v[212:215], v201 offset:50176
	ds_read_b128 v[216:219], v201 offset:51200
	ds_read_b128 v[220:223], v201 offset:52224
	ds_read_b128 v[224:227], v201 offset:53248
	ds_read_b128 v[228:231], v201 offset:54272
	ds_read_b128 v[232:235], v201 offset:55296
	ds_read_b128 v[236:239], v201 offset:56320
	global_load_lds_dwordx4 v[184:185], off
	s_add_i32 m0, s28, 0x2000
	s_add_u32 s26, s26, 0x4080
	v_lshl_add_u64 v[184:185], v[186:187], 0, s[12:13]
	s_addc_u32 s27, s27, 0
	s_add_i32 s28, s34, s2
	global_load_lds_dwordx4 v[184:185], off
	v_lshl_add_u64 v[184:185], s[26:27], 0, v[160:161]
	s_mov_b32 m0, s28
	s_nop 0
	global_load_lds_dwordx4 v[184:185], off
	v_lshl_add_u64 v[184:185], s[26:27], 0, v[162:163]
	s_add_i32 m0, s28, 0x2000
	s_nop 0
	global_load_lds_dwordx4 v[184:185], off
	v_lshl_add_u64 v[184:185], v[190:191], 0, s[12:13]
	s_mov_b32 m0, s40
	s_nop 0
	global_load_lds_dwordx4 v[184:185], off
	v_lshl_add_u64 v[184:185], v[188:189], 0, s[12:13]
	s_mov_b32 m0, s41
	s_nop 0
	global_load_lds_dwordx4 v[184:185], off
	s_waitcnt vmcnt(8)
	s_waitcnt lgkmcnt(0)
	s_barrier
	s_setprio 1
	s_nop 1
	s_waitcnt lgkmcnt(0)
	v_mfma_scale_f32_16x16x128_f8f6f4 v[92:95], v[0:7], v[208:215], v[92:95], v197, v196 op_sel_hi:[0,0,0]
	v_mfma_scale_f32_16x16x128_f8f6f4 v[88:91], v[8:15], v[208:215], v[88:91], v197, v196 op_sel_hi:[0,0,0]
	v_mfma_scale_f32_16x16x128_f8f6f4 v[64:67], v[8:15], v[216:223], v[64:67], v197, v196 op_sel_hi:[0,0,0]
	v_mfma_scale_f32_16x16x128_f8f6f4 v[68:71], v[0:7], v[216:223], v[68:71], v197, v196 op_sel_hi:[0,0,0]
	v_mfma_scale_f32_16x16x128_f8f6f4 v[44:47], v[0:7], v[224:231], v[44:47], v197, v196 op_sel_hi:[0,0,0]
	v_mfma_scale_f32_16x16x128_f8f6f4 v[40:43], v[8:15], v[224:231], v[40:43], v197, v196 op_sel_hi:[0,0,0]
	v_mfma_scale_f32_16x16x128_f8f6f4 v[32:35], v[8:15], v[232:239], v[32:35], v197, v196 op_sel_hi:[0,0,0]
	v_mfma_scale_f32_16x16x128_f8f6f4 v[36:39], v[0:7], v[232:239], v[36:39], v197, v196 op_sel_hi:[0,0,0]
	s_setprio 0
	s_setprio 1
	v_mfma_scale_f32_16x16x128_f8f6f4 v[56:59], v[16:23], v[232:239], v[56:59], v197, v196 op_sel_hi:[0,0,0]
	v_mfma_scale_f32_16x16x128_f8f6f4 v[60:63], v[24:31], v[232:239], v[60:63], v197, v196 op_sel_hi:[0,0,0]
	v_mfma_scale_f32_16x16x128_f8f6f4 v[76:79], v[24:31], v[224:231], v[76:79], v197, v196 op_sel_hi:[0,0,0]
	v_mfma_scale_f32_16x16x128_f8f6f4 v[72:75], v[16:23], v[224:231], v[72:75], v197, v196 op_sel_hi:[0,0,0]
	v_mfma_scale_f32_16x16x128_f8f6f4 v[52:55], v[16:23], v[216:223], v[52:55], v197, v196 op_sel_hi:[0,0,0]
	v_mfma_scale_f32_16x16x128_f8f6f4 v[48:51], v[24:31], v[216:223], v[48:51], v197, v196 op_sel_hi:[0,0,0]
	v_mfma_scale_f32_16x16x128_f8f6f4 v[80:83], v[24:31], v[208:215], v[80:83], v197, v196 op_sel_hi:[0,0,0]
	v_mfma_scale_f32_16x16x128_f8f6f4 v[84:87], v[16:23], v[208:215], v[84:87], v197, v196 op_sel_hi:[0,0,0]
	s_setprio 0
	s_barrier
	s_add_i32 s30, s30, 2
	s_cmp_gt_u32 s30, 13
	s_mov_b64 s[28:29], s[6:7]
	s_cbranch_scc0 .LBB0_182
	s_nop 15
	s_nop 15
	s_and_b64 vcc, exec, s[16:17]
	s_cbranch_vccz .LBB0_185
	s_barrier

.LBB0_813:
	s_add_i32 s10, s1, -7
	s_add_i32 s2, s1, 2
	s_lshl_b64 s[28:29], s[10:11], 7
	s_add_u32 s46, s28, 0x4000000
	s_addc_u32 s47, s29, 0
	v_sub_co_u32_e64 v0, s[28:29], s1, 6
	s_nop 0
	v_readfirstlane_b32 s10, v0
	s_lshl_b64 s[30:31], s[10:11], 7
	s_add_u32 s10, s30, 0x4000000
	s_addc_u32 s23, s31, 0
	s_add_u32 s30, s30, 0x400000
	s_addc_u32 s31, s31, 0
	s_and_b64 s[28:29], s[28:29], exec
	s_cselect_b32 s29, s26, s30
	s_cselect_b32 s28, s27, s31
	s_cselect_b32 s23, s27, s23
	s_cselect_b32 s10, s26, s10
	s_add_u32 s30, s24, s29
	s_addc_u32 s31, s25, s28
	s_cmp_eq_u32 s1, 14
	s_cselect_b64 vcc, -1, 0
	s_and_b64 s[28:29], vcc, exec
	s_cselect_b32 s29, s7, s31
	s_cselect_b32 s28, s6, s30
	s_cselect_b32 s10, 0, s10
	s_cselect_b32 s23, 0, s23
	s_add_i32 s30, 0, 0x10000
	v_add_u32_e32 v0, s30, v171
	v_add_u32_e32 v20, s43, v171
	ds_read_b128 v[8:11], v0
	ds_read_b128 v[12:15], v0 offset:1024
	ds_read_b128 v[24:27], v0 offset:2048
	ds_read_b128 v[28:31], v0 offset:3072
	ds_read_b128 v[0:3], v20
	ds_read_b128 v[4:7], v20 offset:1024
	ds_read_b128 v[16:19], v20 offset:2048
	ds_read_b128 v[20:23], v20 offset:3072
	s_add_u32 s31, s26, 0xffffff80
	s_addc_u32 s48, s27, -1
	s_cmp_lt_u32 s1, 8
	v_cndmask_b32_e32 v32, v198, v194, vcc
	v_cndmask_b32_e32 v180, v170, v195, vcc
	v_cndmask_b32_e32 v201, v172, v196, vcc
	v_cndmask_b32_e32 v234, v174, v197, vcc
	s_cselect_b32 s47, s48, s47
	s_cselect_b32 s31, s31, s46
	s_add_u32 s46, s8, s31
	s_addc_u32 s47, s9, s47
	v_lshl_add_u64 v[176:177], s[46:47], 0, v[172:173]
	s_add_i32 m0, s36, 0xc000
	ds_read_b128 v[202:205], v193
	ds_read_b128 v[206:209], v193 offset:1024
	ds_read_b128 v[210:213], v193 offset:2048
	ds_read_b128 v[214:217], v193 offset:3072
	ds_read_b128 v[218:221], v193 offset:4096
	ds_read_b128 v[222:225], v193 offset:5120
	ds_read_b128 v[226:229], v193 offset:6144
	ds_read_b128 v[230:233], v193 offset:7168
	global_load_lds_dwordx4 v[176:177], off
	v_lshl_add_u64 v[176:177], s[46:47], 0, v[174:175]
	s_add_i32 m0, s36, 0xe000
	s_nop 0
	global_load_lds_dwordx4 v[176:177], off
	s_waitcnt vmcnt(8)
	s_waitcnt lgkmcnt(0)
	s_barrier
	s_setprio 1
	s_nop 1
	s_waitcnt lgkmcnt(0)
	v_mfma_scale_f32_16x16x128_f8f6f4 v[158:161], v[8:15], v[202:209], v[158:161], v189, v188 op_sel_hi:[0,0,0]
	v_mfma_scale_f32_16x16x128_f8f6f4 v[154:157], v[24:31], v[202:209], v[154:157], v189, v188 op_sel_hi:[0,0,0]
	v_mfma_scale_f32_16x16x128_f8f6f4 v[138:141], v[24:31], v[210:217], v[138:141], v189, v188 op_sel_hi:[0,0,0]
	v_mfma_scale_f32_16x16x128_f8f6f4 v[142:145], v[8:15], v[210:217], v[142:145], v189, v188 op_sel_hi:[0,0,0]
	v_mfma_scale_f32_16x16x128_f8f6f4 v[126:129], v[8:15], v[218:225], v[126:129], v189, v188 op_sel_hi:[0,0,0]
	v_mfma_scale_f32_16x16x128_f8f6f4 v[122:125], v[24:31], v[218:225], v[122:125], v189, v188 op_sel_hi:[0,0,0]
	v_mfma_scale_f32_16x16x128_f8f6f4 v[106:109], v[24:31], v[226:233], v[106:109], v189, v188 op_sel_hi:[0,0,0]
	v_mfma_scale_f32_16x16x128_f8f6f4 v[110:113], v[8:15], v[226:233], v[110:113], v189, v188 op_sel_hi:[0,0,0]
	s_setprio 0
	s_setprio 1
	v_mfma_scale_f32_16x16x128_f8f6f4 v[102:105], v[0:7], v[226:233], v[102:105], v189, v188 op_sel_hi:[0,0,0]
	v_mfma_scale_f32_16x16x128_f8f6f4 v[98:101], v[16:23], v[226:233], v[98:101], v189, v188 op_sel_hi:[0,0,0]
	v_mfma_scale_f32_16x16x128_f8f6f4 v[114:117], v[16:23], v[218:225], v[114:117], v189, v188 op_sel_hi:[0,0,0]
	v_mfma_scale_f32_16x16x128_f8f6f4 v[118:121], v[0:7], v[218:225], v[118:121], v189, v188 op_sel_hi:[0,0,0]
	v_mfma_scale_f32_16x16x128_f8f6f4 v[134:137], v[0:7], v[210:217], v[134:137], v189, v188 op_sel_hi:[0,0,0]
	v_mfma_scale_f32_16x16x128_f8f6f4 v[130:133], v[16:23], v[210:217], v[130:133], v189, v188 op_sel_hi:[0,0,0]
	v_mfma_scale_f32_16x16x128_f8f6f4 v[146:149], v[16:23], v[202:209], v[146:149], v189, v188 op_sel_hi:[0,0,0]
	v_mfma_scale_f32_16x16x128_f8f6f4 v[150:153], v[0:7], v[202:209], v[150:153], v189, v188 op_sel_hi:[0,0,0]
	s_setprio 0
	s_barrier
	s_add_i32 s30, s30, s35
	v_lshl_add_u64 v[176:177], s[28:29], 0, v[162:163]
	s_mov_b32 m0, s30
	ds_read_b128 v[202:205], v193 offset:16384
	ds_read_b128 v[206:209], v193 offset:17408
	ds_read_b128 v[210:213], v193 offset:18432
	ds_read_b128 v[214:217], v193 offset:19456
	ds_read_b128 v[218:221], v193 offset:20480
	ds_read_b128 v[222:225], v193 offset:21504
	ds_read_b128 v[226:229], v193 offset:22528
	ds_read_b128 v[230:233], v193 offset:23552
	global_load_lds_dwordx4 v[176:177], off
	s_add_i32 m0, s30, 0x2000
	s_add_u32 s30, s28, 0x2000
	v_lshl_add_u64 v[178:179], s[28:29], 0, v[164:165]
	s_addc_u32 s31, s29, 0
	s_add_i32 s46, s43, s35
	global_load_lds_dwordx4 v[178:179], off
	v_lshl_add_u64 v[182:183], s[30:31], 0, v[162:163]
	s_mov_b32 m0, s46
	v_mov_b32_e32 v181, v33
	global_load_lds_dwordx4 v[182:183], off
	s_add_i32 m0, s46, 0x2000
	v_lshl_add_u64 v[182:183], s[30:31], 0, v[164:165]
	s_add_u32 s30, s8, s10
	global_load_lds_dwordx4 v[182:183], off
	s_addc_u32 s31, s9, s23
	s_mov_b32 m0, s36
	v_lshl_add_u64 v[182:183], s[30:31], 0, v[32:33]
	global_load_lds_dwordx4 v32, s[30:31]
	s_mov_b32 m0, s37
	s_nop 0
	global_load_lds_dwordx4 v180, s[30:31]
	s_waitcnt vmcnt(8)
	s_waitcnt lgkmcnt(0)
	v_lshl_add_u64 v[180:181], s[30:31], 0, v[180:181]
	s_barrier
	s_setprio 1
	s_nop 1
	s_waitcnt lgkmcnt(0)
	v_mfma_scale_f32_16x16x128_f8f6f4 v[94:97], v[8:15], v[202:209], v[94:97], v189, v188 op_sel_hi:[0,0,0]
	v_mfma_scale_f32_16x16x128_f8f6f4 v[90:93], v[24:31], v[202:209], v[90:93], v189, v188 op_sel_hi:[0,0,0]
	v_mfma_scale_f32_16x16x128_f8f6f4 v[74:77], v[24:31], v[210:217], v[74:77], v189, v188 op_sel_hi:[0,0,0]
	v_mfma_scale_f32_16x16x128_f8f6f4 v[78:81], v[8:15], v[210:217], v[78:81], v189, v188 op_sel_hi:[0,0,0]
	v_mfma_scale_f32_16x16x128_f8f6f4 v[62:65], v[8:15], v[218:225], v[62:65], v189, v188 op_sel_hi:[0,0,0]
	v_mfma_scale_f32_16x16x128_f8f6f4 v[58:61], v[24:31], v[218:225], v[58:61], v189, v188 op_sel_hi:[0,0,0]
	v_mfma_scale_f32_16x16x128_f8f6f4 v[42:45], v[24:31], v[226:233], v[42:45], v189, v188 op_sel_hi:[0,0,0]
	v_mfma_scale_f32_16x16x128_f8f6f4 v[46:49], v[8:15], v[226:233], v[46:49], v189, v188 op_sel_hi:[0,0,0]
	s_setprio 0
	s_setprio 1
	v_mfma_scale_f32_16x16x128_f8f6f4 v[38:41], v[0:7], v[226:233], v[38:41], v189, v188 op_sel_hi:[0,0,0]
	v_mfma_scale_f32_16x16x128_f8f6f4 v[34:37], v[16:23], v[226:233], v[34:37], v189, v188 op_sel_hi:[0,0,0]
	v_mfma_scale_f32_16x16x128_f8f6f4 v[50:53], v[16:23], v[218:225], v[50:53], v189, v188 op_sel_hi:[0,0,0]
	v_mfma_scale_f32_16x16x128_f8f6f4 v[54:57], v[0:7], v[218:225], v[54:57], v189, v188 op_sel_hi:[0,0,0]
	v_mfma_scale_f32_16x16x128_f8f6f4 v[70:73], v[0:7], v[210:217], v[70:73], v189, v188 op_sel_hi:[0,0,0]
	v_mfma_scale_f32_16x16x128_f8f6f4 v[66:69], v[16:23], v[210:217], v[66:69], v189, v188 op_sel_hi:[0,0,0]
	v_mfma_scale_f32_16x16x128_f8f6f4 v[82:85], v[16:23], v[202:209], v[82:85], v189, v188 op_sel_hi:[0,0,0]
	v_mfma_scale_f32_16x16x128_f8f6f4 v[86:89], v[0:7], v[202:209], v[86:89], v189, v188 op_sel_hi:[0,0,0]
	s_setprio 0
	s_barrier
	s_add_i32 s10, 0, 0x18000
	s_add_i32 s23, 0, 0x1c000
	v_add_u32_e32 v0, s10, v171
	v_add_u32_e32 v12, s23, v171
	ds_read_b128 v[16:19], v0
	ds_read_b128 v[20:23], v0 offset:1024
	ds_read_b128 v[24:27], v0 offset:2048
	ds_read_b128 v[28:31], v0 offset:3072
	ds_read_b128 v[0:3], v12
	ds_read_b128 v[4:7], v12 offset:1024
	ds_read_b128 v[8:11], v12 offset:2048
	ds_read_b128 v[12:15], v12 offset:3072
	s_mov_b32 m0, s38
	ds_read_b128 v[202:205], v193 offset:32768
	ds_read_b128 v[206:209], v193 offset:33792
	ds_read_b128 v[210:213], v193 offset:34816
	ds_read_b128 v[214:217], v193 offset:35840
	ds_read_b128 v[218:221], v193 offset:36864
	ds_read_b128 v[222:225], v193 offset:37888
	ds_read_b128 v[226:229], v193 offset:38912
	ds_read_b128 v[230:233], v193 offset:39936
	global_load_lds_dwordx4 v201, s[30:31]
	s_mov_b32 m0, s39
	s_nop 0
	global_load_lds_dwordx4 v234, s[30:31]
	s_waitcnt vmcnt(8)
	s_waitcnt lgkmcnt(0)
	s_barrier
	s_setprio 1
	s_nop 1
	s_waitcnt lgkmcnt(0)
	v_mfma_scale_f32_16x16x128_f8f6f4 v[158:161], v[16:23], v[202:209], v[158:161], v189, v188 op_sel_hi:[0,0,0]
	v_mfma_scale_f32_16x16x128_f8f6f4 v[154:157], v[24:31], v[202:209], v[154:157], v189, v188 op_sel_hi:[0,0,0]
	v_mfma_scale_f32_16x16x128_f8f6f4 v[138:141], v[24:31], v[210:217], v[138:141], v189, v188 op_sel_hi:[0,0,0]
	v_mfma_scale_f32_16x16x128_f8f6f4 v[142:145], v[16:23], v[210:217], v[142:145], v189, v188 op_sel_hi:[0,0,0]
	v_mfma_scale_f32_16x16x128_f8f6f4 v[126:129], v[16:23], v[218:225], v[126:129], v189, v188 op_sel_hi:[0,0,0]
	v_mfma_scale_f32_16x16x128_f8f6f4 v[122:125], v[24:31], v[218:225], v[122:125], v189, v188 op_sel_hi:[0,0,0]
	v_mfma_scale_f32_16x16x128_f8f6f4 v[106:109], v[24:31], v[226:233], v[106:109], v189, v188 op_sel_hi:[0,0,0]
	v_mfma_scale_f32_16x16x128_f8f6f4 v[110:113], v[16:23], v[226:233], v[110:113], v189, v188 op_sel_hi:[0,0,0]
	s_setprio 0
	s_setprio 1
	v_mfma_scale_f32_16x16x128_f8f6f4 v[102:105], v[0:7], v[226:233], v[102:105], v189, v188 op_sel_hi:[0,0,0]
	v_mfma_scale_f32_16x16x128_f8f6f4 v[98:101], v[8:15], v[226:233], v[98:101], v189, v188 op_sel_hi:[0,0,0]
	v_mfma_scale_f32_16x16x128_f8f6f4 v[114:117], v[8:15], v[218:225], v[114:117], v189, v188 op_sel_hi:[0,0,0]
	v_mfma_scale_f32_16x16x128_f8f6f4 v[118:121], v[0:7], v[218:225], v[118:121], v189, v188 op_sel_hi:[0,0,0]
	v_mfma_scale_f32_16x16x128_f8f6f4 v[134:137], v[0:7], v[210:217], v[134:137], v189, v188 op_sel_hi:[0,0,0]
	v_mfma_scale_f32_16x16x128_f8f6f4 v[130:133], v[8:15], v[210:217], v[130:133], v189, v188 op_sel_hi:[0,0,0]
	v_mfma_scale_f32_16x16x128_f8f6f4 v[146:149], v[8:15], v[202:209], v[146:149], v189, v188 op_sel_hi:[0,0,0]
	v_mfma_scale_f32_16x16x128_f8f6f4 v[150:153], v[0:7], v[202:209], v[150:153], v189, v188 op_sel_hi:[0,0,0]
	s_setprio 0
	s_barrier
	s_add_i32 s10, s10, s35
	v_lshl_add_u64 v[176:177], v[176:177], 0, s[18:19]
	s_mov_b32 m0, s10
	ds_read_b128 v[202:205], v193 offset:49152
	ds_read_b128 v[206:209], v193 offset:50176
	ds_read_b128 v[210:213], v193 offset:51200
	ds_read_b128 v[214:217], v193 offset:52224
	ds_read_b128 v[218:221], v193 offset:53248
	ds_read_b128 v[222:225], v193 offset:54272
	ds_read_b128 v[226:229], v193 offset:55296
	ds_read_b128 v[230:233], v193 offset:56320
	global_load_lds_dwordx4 v[176:177], off
	s_add_i32 m0, s10, 0x2000
	s_add_u32 s28, s28, 0x2080
	v_lshl_add_u64 v[176:177], v[178:179], 0, s[18:19]
	s_addc_u32 s29, s29, 0
	s_add_i32 s10, s23, s35
	global_load_lds_dwordx4 v[176:177], off
	v_lshl_add_u64 v[176:177], s[28:29], 0, v[162:163]
	s_mov_b32 m0, s10
	s_nop 0
	global_load_lds_dwordx4 v[176:177], off
	v_lshl_add_u64 v[176:177], s[28:29], 0, v[164:165]
	s_add_i32 m0, s10, 0x2000
	s_nop 0
	global_load_lds_dwordx4 v[176:177], off
	v_lshl_add_u64 v[176:177], v[182:183], 0, s[18:19]
	s_mov_b32 m0, s40
	s_nop 0
	global_load_lds_dwordx4 v[176:177], off
	v_lshl_add_u64 v[176:177], v[180:181], 0, s[18:19]
	s_mov_b32 m0, s41
	s_nop 0
	global_load_lds_dwordx4 v[176:177], off
	s_waitcnt vmcnt(8)
	s_waitcnt lgkmcnt(0)
	s_barrier
	s_setprio 1
	s_nop 1
	s_waitcnt lgkmcnt(0)
	v_mfma_scale_f32_16x16x128_f8f6f4 v[94:97], v[16:23], v[202:209], v[94:97], v189, v188 op_sel_hi:[0,0,0]
	v_mfma_scale_f32_16x16x128_f8f6f4 v[90:93], v[24:31], v[202:209], v[90:93], v189, v188 op_sel_hi:[0,0,0]
	v_mfma_scale_f32_16x16x128_f8f6f4 v[74:77], v[24:31], v[210:217], v[74:77], v189, v188 op_sel_hi:[0,0,0]
	v_mfma_scale_f32_16x16x128_f8f6f4 v[78:81], v[16:23], v[210:217], v[78:81], v189, v188 op_sel_hi:[0,0,0]
	v_mfma_scale_f32_16x16x128_f8f6f4 v[62:65], v[16:23], v[218:225], v[62:65], v189, v188 op_sel_hi:[0,0,0]
	v_mfma_scale_f32_16x16x128_f8f6f4 v[58:61], v[24:31], v[218:225], v[58:61], v189, v188 op_sel_hi:[0,0,0]
	v_mfma_scale_f32_16x16x128_f8f6f4 v[42:45], v[24:31], v[226:233], v[42:45], v189, v188 op_sel_hi:[0,0,0]
	v_mfma_scale_f32_16x16x128_f8f6f4 v[46:49], v[16:23], v[226:233], v[46:49], v189, v188 op_sel_hi:[0,0,0]
	s_setprio 0
	s_setprio 1
	v_mfma_scale_f32_16x16x128_f8f6f4 v[38:41], v[0:7], v[226:233], v[38:41], v189, v188 op_sel_hi:[0,0,0]
	v_mfma_scale_f32_16x16x128_f8f6f4 v[34:37], v[8:15], v[226:233], v[34:37], v189, v188 op_sel_hi:[0,0,0]
	v_mfma_scale_f32_16x16x128_f8f6f4 v[50:53], v[8:15], v[218:225], v[50:53], v189, v188 op_sel_hi:[0,0,0]
	v_mfma_scale_f32_16x16x128_f8f6f4 v[54:57], v[0:7], v[218:225], v[54:57], v189, v188 op_sel_hi:[0,0,0]
	v_mfma_scale_f32_16x16x128_f8f6f4 v[70:73], v[0:7], v[210:217], v[70:73], v189, v188 op_sel_hi:[0,0,0]
	v_mfma_scale_f32_16x16x128_f8f6f4 v[66:69], v[8:15], v[210:217], v[66:69], v189, v188 op_sel_hi:[0,0,0]
	v_mfma_scale_f32_16x16x128_f8f6f4 v[82:85], v[8:15], v[202:209], v[82:85], v189, v188 op_sel_hi:[0,0,0]
	v_mfma_scale_f32_16x16x128_f8f6f4 v[86:89], v[0:7], v[202:209], v[86:89], v189, v188 op_sel_hi:[0,0,0]
	s_setprio 0
	s_barrier
	s_add_u32 s26, s26, 0x100
	s_addc_u32 s27, s27, 0
	s_cmp_gt_u32 s1, 13
	s_mov_b32 s1, s2
	s_cbranch_scc1 .LBB0_819

.LBB0_901:
	ds_read_b128 v[16:19], v196
	ds_read_b128 v[20:23], v196 offset:1024
	ds_read_b128 v[24:27], v196 offset:2048
	ds_read_b128 v[28:31], v196 offset:3072
	ds_read_b128 v[0:3], v197
	ds_read_b128 v[4:7], v197 offset:1024
	ds_read_b128 v[8:11], v197 offset:2048
	ds_read_b128 v[12:15], v197 offset:3072
	s_add_u32 s34, s38, 0x100
	s_addc_u32 s35, s39, 0
	s_add_u32 s54, s31, s38
	s_addc_u32 s55, s52, s39
	s_cmpk_eq_i32 s38, 0x700
	s_cselect_b64 vcc, -1, 0
	s_and_b64 s[36:37], vcc, exec
	v_cndmask_b32_e32 v164, v203, v199, vcc
	s_cselect_b32 s37, s7, s55
	s_cselect_b32 s36, s6, s54
	v_cndmask_b32_e32 v184, v170, v200, vcc
	v_cndmask_b32_e32 v173, v172, v201, vcc
	v_cndmask_b32_e32 v175, v174, v202, vcc
	s_cselect_b32 s54, 0, s35
	s_cselect_b32 s55, 0, s34
	v_lshl_add_u64 v[180:181], v[178:179], 0, s[38:39]
	s_add_i32 m0, s33, 0xc000
	ds_read_b128 v[204:207], v198
	ds_read_b128 v[208:211], v198 offset:1024
	ds_read_b128 v[212:215], v198 offset:2048
	ds_read_b128 v[216:219], v198 offset:3072
	ds_read_b128 v[220:223], v198 offset:4096
	ds_read_b128 v[224:227], v198 offset:5120
	ds_read_b128 v[228:231], v198 offset:6144
	ds_read_b128 v[232:235], v198 offset:7168
	global_load_lds_dwordx4 v[180:181], off
	v_lshl_add_u64 v[180:181], v[176:177], 0, s[38:39]
	s_add_i32 m0, s33, 0xe000
	s_nop 0
	global_load_lds_dwordx4 v[180:181], off
	s_waitcnt vmcnt(8)
	s_waitcnt lgkmcnt(0)
	s_barrier
	s_setprio 1
	s_nop 1
	s_waitcnt lgkmcnt(0)
	v_mfma_scale_f32_16x16x128_f8f6f4 v[156:159], v[16:23], v[204:211], v[156:159], v193, v192 op_sel_hi:[0,0,0]
	v_mfma_scale_f32_16x16x128_f8f6f4 v[152:155], v[24:31], v[204:211], v[152:155], v193, v192 op_sel_hi:[0,0,0]
	v_mfma_scale_f32_16x16x128_f8f6f4 v[136:139], v[24:31], v[212:219], v[136:139], v193, v192 op_sel_hi:[0,0,0]
	v_mfma_scale_f32_16x16x128_f8f6f4 v[140:143], v[16:23], v[212:219], v[140:143], v193, v192 op_sel_hi:[0,0,0]
	v_mfma_scale_f32_16x16x128_f8f6f4 v[124:127], v[16:23], v[220:227], v[124:127], v193, v192 op_sel_hi:[0,0,0]
	v_mfma_scale_f32_16x16x128_f8f6f4 v[120:123], v[24:31], v[220:227], v[120:123], v193, v192 op_sel_hi:[0,0,0]
	v_mfma_scale_f32_16x16x128_f8f6f4 v[104:107], v[24:31], v[228:235], v[104:107], v193, v192 op_sel_hi:[0,0,0]
	v_mfma_scale_f32_16x16x128_f8f6f4 v[108:111], v[16:23], v[228:235], v[108:111], v193, v192 op_sel_hi:[0,0,0]
	s_setprio 0
	s_setprio 1
	v_mfma_scale_f32_16x16x128_f8f6f4 v[100:103], v[0:7], v[228:235], v[100:103], v193, v192 op_sel_hi:[0,0,0]
	v_mfma_scale_f32_16x16x128_f8f6f4 v[96:99], v[8:15], v[228:235], v[96:99], v193, v192 op_sel_hi:[0,0,0]
	v_mfma_scale_f32_16x16x128_f8f6f4 v[112:115], v[8:15], v[220:227], v[112:115], v193, v192 op_sel_hi:[0,0,0]
	v_mfma_scale_f32_16x16x128_f8f6f4 v[116:119], v[0:7], v[220:227], v[116:119], v193, v192 op_sel_hi:[0,0,0]
	v_mfma_scale_f32_16x16x128_f8f6f4 v[132:135], v[0:7], v[212:219], v[132:135], v193, v192 op_sel_hi:[0,0,0]
	v_mfma_scale_f32_16x16x128_f8f6f4 v[128:131], v[8:15], v[212:219], v[128:131], v193, v192 op_sel_hi:[0,0,0]
	v_mfma_scale_f32_16x16x128_f8f6f4 v[144:147], v[8:15], v[204:211], v[144:147], v193, v192 op_sel_hi:[0,0,0]
	v_mfma_scale_f32_16x16x128_f8f6f4 v[148:151], v[0:7], v[204:211], v[148:151], v193, v192 op_sel_hi:[0,0,0]
	s_setprio 0
	s_barrier
	s_add_i32 s38, s47, s3
	v_lshl_add_u64 v[180:181], s[36:37], 0, v[160:161]
	s_mov_b32 m0, s38
	ds_read_b128 v[204:207], v198 offset:16384
	ds_read_b128 v[208:211], v198 offset:17408
	ds_read_b128 v[212:215], v198 offset:18432
	ds_read_b128 v[216:219], v198 offset:19456
	ds_read_b128 v[220:223], v198 offset:20480
	ds_read_b128 v[224:227], v198 offset:21504
	ds_read_b128 v[228:231], v198 offset:22528
	ds_read_b128 v[232:235], v198 offset:23552
	global_load_lds_dwordx4 v[180:181], off
	s_add_i32 m0, s38, 0x2000
	s_add_u32 s38, s36, 0x40000
	v_lshl_add_u64 v[182:183], s[36:37], 0, v[162:163]
	s_addc_u32 s39, s37, 0
	s_add_i32 s56, s48, s3
	global_load_lds_dwordx4 v[182:183], off
	v_lshl_add_u64 v[186:187], s[38:39], 0, v[160:161]
	s_mov_b32 m0, s56
	v_mov_b32_e32 v185, v165
	global_load_lds_dwordx4 v[186:187], off
	s_add_i32 m0, s56, 0x2000
	v_lshl_add_u64 v[186:187], s[38:39], 0, v[162:163]
	s_add_u32 s38, s10, s55
	global_load_lds_dwordx4 v[186:187], off
	s_addc_u32 s39, s11, s54
	s_mov_b32 m0, s33
	v_lshl_add_u64 v[186:187], s[38:39], 0, v[164:165]
	global_load_lds_dwordx4 v164, s[38:39]
	s_mov_b32 m0, s40
	s_nop 0
	global_load_lds_dwordx4 v184, s[38:39]
	s_waitcnt vmcnt(8)
	s_waitcnt lgkmcnt(0)
	v_lshl_add_u64 v[184:185], s[38:39], 0, v[184:185]
	s_barrier
	s_setprio 1
	s_nop 1
	s_waitcnt lgkmcnt(0)
	v_mfma_scale_f32_16x16x128_f8f6f4 v[92:95], v[16:23], v[204:211], v[92:95], v193, v192 op_sel_hi:[0,0,0]
	v_mfma_scale_f32_16x16x128_f8f6f4 v[88:91], v[24:31], v[204:211], v[88:91], v193, v192 op_sel_hi:[0,0,0]
	v_mfma_scale_f32_16x16x128_f8f6f4 v[72:75], v[24:31], v[212:219], v[72:75], v193, v192 op_sel_hi:[0,0,0]
	v_mfma_scale_f32_16x16x128_f8f6f4 v[76:79], v[16:23], v[212:219], v[76:79], v193, v192 op_sel_hi:[0,0,0]
	v_mfma_scale_f32_16x16x128_f8f6f4 v[52:55], v[16:23], v[220:227], v[52:55], v193, v192 op_sel_hi:[0,0,0]
	v_mfma_scale_f32_16x16x128_f8f6f4 v[48:51], v[24:31], v[220:227], v[48:51], v193, v192 op_sel_hi:[0,0,0]
	v_mfma_scale_f32_16x16x128_f8f6f4 v[32:35], v[24:31], v[228:235], v[32:35], v193, v192 op_sel_hi:[0,0,0]
	v_mfma_scale_f32_16x16x128_f8f6f4 v[36:39], v[16:23], v[228:235], v[36:39], v193, v192 op_sel_hi:[0,0,0]
	s_setprio 0
	s_setprio 1
	v_mfma_scale_f32_16x16x128_f8f6f4 v[40:43], v[0:7], v[228:235], v[40:43], v193, v192 op_sel_hi:[0,0,0]
	v_mfma_scale_f32_16x16x128_f8f6f4 v[44:47], v[8:15], v[228:235], v[44:47], v193, v192 op_sel_hi:[0,0,0]
	v_mfma_scale_f32_16x16x128_f8f6f4 v[68:71], v[8:15], v[220:227], v[68:71], v193, v192 op_sel_hi:[0,0,0]
	v_mfma_scale_f32_16x16x128_f8f6f4 v[64:67], v[0:7], v[220:227], v[64:67], v193, v192 op_sel_hi:[0,0,0]
	v_mfma_scale_f32_16x16x128_f8f6f4 v[60:63], v[0:7], v[212:219], v[60:63], v193, v192 op_sel_hi:[0,0,0]
	v_mfma_scale_f32_16x16x128_f8f6f4 v[56:59], v[8:15], v[212:219], v[56:59], v193, v192 op_sel_hi:[0,0,0]
	v_mfma_scale_f32_16x16x128_f8f6f4 v[80:83], v[8:15], v[204:211], v[80:83], v193, v192 op_sel_hi:[0,0,0]
	v_mfma_scale_f32_16x16x128_f8f6f4 v[84:87], v[0:7], v[204:211], v[84:87], v193, v192 op_sel_hi:[0,0,0]
	s_setprio 0
	s_barrier
	s_add_i32 s54, 0, 0x18000
	s_add_i32 s55, 0, 0x1c000
	v_add_u32_e32 v12, s54, v194
	v_add_u32_e32 v28, s55, v194
	ds_read_b128 v[0:3], v12
	ds_read_b128 v[4:7], v12 offset:1024
	ds_read_b128 v[8:11], v12 offset:2048
	ds_read_b128 v[12:15], v12 offset:3072
	ds_read_b128 v[16:19], v28
	ds_read_b128 v[20:23], v28 offset:1024
	ds_read_b128 v[24:27], v28 offset:2048
	ds_read_b128 v[28:31], v28 offset:3072
	s_mov_b32 m0, s41
	ds_read_b128 v[204:207], v198 offset:32768
	ds_read_b128 v[208:211], v198 offset:33792
	ds_read_b128 v[212:215], v198 offset:34816
	ds_read_b128 v[216:219], v198 offset:35840
	ds_read_b128 v[220:223], v198 offset:36864
	ds_read_b128 v[224:227], v198 offset:37888
	ds_read_b128 v[228:231], v198 offset:38912
	ds_read_b128 v[232:235], v198 offset:39936
	global_load_lds_dwordx4 v173, s[38:39]
	s_mov_b32 m0, s42
	s_nop 0
	global_load_lds_dwordx4 v175, s[38:39]
	s_waitcnt vmcnt(8)
	s_waitcnt lgkmcnt(0)
	s_barrier
	s_setprio 1
	s_nop 1
	s_waitcnt lgkmcnt(0)
	v_mfma_scale_f32_16x16x128_f8f6f4 v[156:159], v[0:7], v[204:211], v[156:159], v193, v192 op_sel_hi:[0,0,0]
	v_mfma_scale_f32_16x16x128_f8f6f4 v[152:155], v[8:15], v[204:211], v[152:155], v193, v192 op_sel_hi:[0,0,0]
	v_mfma_scale_f32_16x16x128_f8f6f4 v[136:139], v[8:15], v[212:219], v[136:139], v193, v192 op_sel_hi:[0,0,0]
	v_mfma_scale_f32_16x16x128_f8f6f4 v[140:143], v[0:7], v[212:219], v[140:143], v193, v192 op_sel_hi:[0,0,0]
	v_mfma_scale_f32_16x16x128_f8f6f4 v[124:127], v[0:7], v[220:227], v[124:127], v193, v192 op_sel_hi:[0,0,0]
	v_mfma_scale_f32_16x16x128_f8f6f4 v[120:123], v[8:15], v[220:227], v[120:123], v193, v192 op_sel_hi:[0,0,0]
	v_mfma_scale_f32_16x16x128_f8f6f4 v[104:107], v[8:15], v[228:235], v[104:107], v193, v192 op_sel_hi:[0,0,0]
	v_mfma_scale_f32_16x16x128_f8f6f4 v[108:111], v[0:7], v[228:235], v[108:111], v193, v192 op_sel_hi:[0,0,0]
	s_setprio 0
	s_setprio 1
	v_mfma_scale_f32_16x16x128_f8f6f4 v[100:103], v[16:23], v[228:235], v[100:103], v193, v192 op_sel_hi:[0,0,0]
	v_mfma_scale_f32_16x16x128_f8f6f4 v[96:99], v[24:31], v[228:235], v[96:99], v193, v192 op_sel_hi:[0,0,0]
	v_mfma_scale_f32_16x16x128_f8f6f4 v[112:115], v[24:31], v[220:227], v[112:115], v193, v192 op_sel_hi:[0,0,0]
	v_mfma_scale_f32_16x16x128_f8f6f4 v[116:119], v[16:23], v[220:227], v[116:119], v193, v192 op_sel_hi:[0,0,0]
	v_mfma_scale_f32_16x16x128_f8f6f4 v[132:135], v[16:23], v[212:219], v[132:135], v193, v192 op_sel_hi:[0,0,0]
	v_mfma_scale_f32_16x16x128_f8f6f4 v[128:131], v[24:31], v[212:219], v[128:131], v193, v192 op_sel_hi:[0,0,0]
	v_mfma_scale_f32_16x16x128_f8f6f4 v[144:147], v[24:31], v[204:211], v[144:147], v193, v192 op_sel_hi:[0,0,0]
	v_mfma_scale_f32_16x16x128_f8f6f4 v[148:151], v[16:23], v[204:211], v[148:151], v193, v192 op_sel_hi:[0,0,0]
	s_setprio 0
	s_barrier
	s_add_i32 s38, s54, s3
	v_lshl_add_u64 v[180:181], v[180:181], 0, s[18:19]
	s_mov_b32 m0, s38
	ds_read_b128 v[204:207], v198 offset:49152
	ds_read_b128 v[208:211], v198 offset:50176
	ds_read_b128 v[212:215], v198 offset:51200
	ds_read_b128 v[216:219], v198 offset:52224
	ds_read_b128 v[220:223], v198 offset:53248
	ds_read_b128 v[224:227], v198 offset:54272
	ds_read_b128 v[228:231], v198 offset:55296
	ds_read_b128 v[232:235], v198 offset:56320
	global_load_lds_dwordx4 v[180:181], off
	s_add_i32 m0, s38, 0x2000
	s_add_u32 s36, s36, 0x40080
	v_lshl_add_u64 v[180:181], v[182:183], 0, s[18:19]
	s_addc_u32 s37, s37, 0
	s_add_i32 s38, s55, s3
	global_load_lds_dwordx4 v[180:181], off
	v_lshl_add_u64 v[180:181], s[36:37], 0, v[160:161]
	s_mov_b32 m0, s38
	s_nop 0
	global_load_lds_dwordx4 v[180:181], off
	v_lshl_add_u64 v[180:181], s[36:37], 0, v[162:163]
	s_add_i32 m0, s38, 0x2000
	s_nop 0
	global_load_lds_dwordx4 v[180:181], off
	v_lshl_add_u64 v[180:181], v[186:187], 0, s[18:19]
	s_mov_b32 m0, s44
	s_nop 0
	global_load_lds_dwordx4 v[180:181], off
	v_lshl_add_u64 v[180:181], v[184:185], 0, s[18:19]
	s_mov_b32 m0, s45
	s_nop 0
	global_load_lds_dwordx4 v[180:181], off
	s_waitcnt vmcnt(8)
	s_waitcnt lgkmcnt(0)
	s_barrier
	s_setprio 1
	s_nop 1
	s_waitcnt lgkmcnt(0)
	v_mfma_scale_f32_16x16x128_f8f6f4 v[92:95], v[0:7], v[204:211], v[92:95], v193, v192 op_sel_hi:[0,0,0]
	v_mfma_scale_f32_16x16x128_f8f6f4 v[88:91], v[8:15], v[204:211], v[88:91], v193, v192 op_sel_hi:[0,0,0]
	v_mfma_scale_f32_16x16x128_f8f6f4 v[72:75], v[8:15], v[212:219], v[72:75], v193, v192 op_sel_hi:[0,0,0]
	v_mfma_scale_f32_16x16x128_f8f6f4 v[76:79], v[0:7], v[212:219], v[76:79], v193, v192 op_sel_hi:[0,0,0]
	v_mfma_scale_f32_16x16x128_f8f6f4 v[52:55], v[0:7], v[220:227], v[52:55], v193, v192 op_sel_hi:[0,0,0]
	v_mfma_scale_f32_16x16x128_f8f6f4 v[48:51], v[8:15], v[220:227], v[48:51], v193, v192 op_sel_hi:[0,0,0]
	v_mfma_scale_f32_16x16x128_f8f6f4 v[32:35], v[8:15], v[228:235], v[32:35], v193, v192 op_sel_hi:[0,0,0]
	v_mfma_scale_f32_16x16x128_f8f6f4 v[36:39], v[0:7], v[228:235], v[36:39], v193, v192 op_sel_hi:[0,0,0]
	s_setprio 0
	s_setprio 1
	v_mfma_scale_f32_16x16x128_f8f6f4 v[40:43], v[16:23], v[228:235], v[40:43], v193, v192 op_sel_hi:[0,0,0]
	v_mfma_scale_f32_16x16x128_f8f6f4 v[44:47], v[24:31], v[228:235], v[44:47], v193, v192 op_sel_hi:[0,0,0]
	v_mfma_scale_f32_16x16x128_f8f6f4 v[68:71], v[24:31], v[220:227], v[68:71], v193, v192 op_sel_hi:[0,0,0]
	v_mfma_scale_f32_16x16x128_f8f6f4 v[64:67], v[16:23], v[220:227], v[64:67], v193, v192 op_sel_hi:[0,0,0]
	v_mfma_scale_f32_16x16x128_f8f6f4 v[60:63], v[16:23], v[212:219], v[60:63], v193, v192 op_sel_hi:[0,0,0]
	v_mfma_scale_f32_16x16x128_f8f6f4 v[56:59], v[24:31], v[212:219], v[56:59], v193, v192 op_sel_hi:[0,0,0]
	v_mfma_scale_f32_16x16x128_f8f6f4 v[80:83], v[24:31], v[204:211], v[80:83], v193, v192 op_sel_hi:[0,0,0]
	v_mfma_scale_f32_16x16x128_f8f6f4 v[84:87], v[16:23], v[204:211], v[84:87], v193, v192 op_sel_hi:[0,0,0]
	s_setprio 0
	s_barrier
	s_add_i32 s53, s53, 2
	s_cmp_gt_u32 s53, 13
	s_mov_b64 s[38:39], s[34:35]
	s_cbranch_scc0 .LBB0_901
	s_nop 15
	s_nop 15
	s_and_b64 vcc, exec, s[22:23]
	s_cbranch_vccz .LBB0_904
	s_barrier

.LBB0_1149:
	s_add_u32 s6, s38, 0x100
	s_addc_u32 s7, s39, 0
	s_cmpk_eq_i32 s38, 0x700
	v_lshl_add_u64 v[0:1], v[184:185], 0, s[38:39]
	s_cselect_b64 vcc, -1, 0
	v_cndmask_b32_e32 v186, v0, v170, vcc
	v_add_u32_e32 v0, s48, v204
	v_add_u32_e32 v12, s49, v204
	v_cndmask_b32_e32 v187, v1, v171, vcc
	ds_read_b128 v[16:19], v0
	ds_read_b128 v[20:23], v0 offset:1024
	ds_read_b128 v[24:27], v0 offset:2048
	ds_read_b128 v[28:31], v0 offset:3072
	ds_read_b128 v[0:3], v12
	ds_read_b128 v[4:7], v12 offset:1024
	ds_read_b128 v[8:11], v12 offset:2048
	ds_read_b128 v[12:15], v12 offset:3072
	s_and_b64 s[56:57], vcc, exec
	v_cndmask_b32_e32 v160, v173, v169, vcc
	v_cndmask_b32_e32 v192, v178, v209, vcc
	v_cndmask_b32_e32 v175, v176, v210, vcc
	v_cndmask_b32_e32 v177, v174, v211, vcc
	s_cselect_b32 s56, 0, s7
	s_cselect_b32 s57, 0, s6
	v_lshl_add_u64 v[188:189], v[182:183], 0, s[38:39]
	s_add_i32 m0, s37, 0xc000
	ds_read_b128 v[212:215], v206
	ds_read_b128 v[216:219], v206 offset:1024
	ds_read_b128 v[220:223], v206 offset:2048
	ds_read_b128 v[224:227], v206 offset:3072
	ds_read_b128 v[228:231], v206 offset:4096
	ds_read_b128 v[232:235], v206 offset:5120
	ds_read_b128 v[236:239], v206 offset:6144
	ds_read_b128 v[240:243], v206 offset:7168
	global_load_lds_dwordx4 v[188:189], off
	v_lshl_add_u64 v[188:189], v[180:181], 0, s[38:39]
	s_add_i32 m0, s37, 0xe000
	s_nop 0
	global_load_lds_dwordx4 v[188:189], off
	s_waitcnt vmcnt(8)
	s_waitcnt lgkmcnt(0)
	s_barrier
	s_setprio 1
	s_nop 1
	s_waitcnt lgkmcnt(0)
	v_mfma_scale_f32_16x16x128_f8f6f4 v[156:159], v[16:23], v[212:219], v[156:159], v199, v198 op_sel_hi:[0,0,0]
	v_mfma_scale_f32_16x16x128_f8f6f4 v[148:151], v[24:31], v[212:219], v[148:151], v199, v198 op_sel_hi:[0,0,0]
	v_mfma_scale_f32_16x16x128_f8f6f4 v[132:135], v[24:31], v[220:227], v[132:135], v199, v198 op_sel_hi:[0,0,0]
	v_mfma_scale_f32_16x16x128_f8f6f4 v[140:143], v[16:23], v[220:227], v[140:143], v199, v198 op_sel_hi:[0,0,0]
	v_mfma_scale_f32_16x16x128_f8f6f4 v[124:127], v[16:23], v[228:235], v[124:127], v199, v198 op_sel_hi:[0,0,0]
	v_mfma_scale_f32_16x16x128_f8f6f4 v[116:119], v[24:31], v[228:235], v[116:119], v199, v198 op_sel_hi:[0,0,0]
	v_mfma_scale_f32_16x16x128_f8f6f4 v[100:103], v[24:31], v[236:243], v[100:103], v199, v198 op_sel_hi:[0,0,0]
	v_mfma_scale_f32_16x16x128_f8f6f4 v[108:111], v[16:23], v[236:243], v[108:111], v199, v198 op_sel_hi:[0,0,0]
	s_setprio 0
	s_setprio 1
	v_mfma_scale_f32_16x16x128_f8f6f4 v[104:107], v[0:7], v[236:243], v[104:107], v199, v198 op_sel_hi:[0,0,0]
	v_mfma_scale_f32_16x16x128_f8f6f4 v[96:99], v[8:15], v[236:243], v[96:99], v199, v198 op_sel_hi:[0,0,0]
	v_mfma_scale_f32_16x16x128_f8f6f4 v[112:115], v[8:15], v[228:235], v[112:115], v199, v198 op_sel_hi:[0,0,0]
	v_mfma_scale_f32_16x16x128_f8f6f4 v[120:123], v[0:7], v[228:235], v[120:123], v199, v198 op_sel_hi:[0,0,0]
	v_mfma_scale_f32_16x16x128_f8f6f4 v[136:139], v[0:7], v[220:227], v[136:139], v199, v198 op_sel_hi:[0,0,0]
	v_mfma_scale_f32_16x16x128_f8f6f4 v[128:131], v[8:15], v[220:227], v[128:131], v199, v198 op_sel_hi:[0,0,0]
	v_mfma_scale_f32_16x16x128_f8f6f4 v[144:147], v[8:15], v[212:219], v[144:147], v199, v198 op_sel_hi:[0,0,0]
	v_mfma_scale_f32_16x16x128_f8f6f4 v[152:155], v[0:7], v[212:219], v[152:155], v199, v198 op_sel_hi:[0,0,0]
	s_setprio 0
	s_barrier
	s_add_i32 s38, s48, s3
	v_lshl_add_u64 v[188:189], v[186:187], 0, v[164:165]
	s_mov_b32 m0, s38
	ds_read_b128 v[212:215], v206 offset:16384
	ds_read_b128 v[216:219], v206 offset:17408
	ds_read_b128 v[220:223], v206 offset:18432
	ds_read_b128 v[224:227], v206 offset:19456
	ds_read_b128 v[228:231], v206 offset:20480
	ds_read_b128 v[232:235], v206 offset:21504
	ds_read_b128 v[236:239], v206 offset:22528
	ds_read_b128 v[240:243], v206 offset:23552
	global_load_lds_dwordx4 v[188:189], off
	v_lshl_add_u64 v[190:191], v[186:187], 0, v[162:163]
	s_add_i32 m0, s38, 0x2000
	v_lshl_add_u64 v[194:195], v[186:187], 0, s[16:17]
	s_add_i32 s38, s49, s3
	global_load_lds_dwordx4 v[190:191], off
	v_lshl_add_u64 v[244:245], v[194:195], 0, v[164:165]
	s_mov_b32 m0, s38
	v_lshl_add_u64 v[194:195], v[194:195], 0, v[162:163]
	global_load_lds_dwordx4 v[244:245], off
	s_add_i32 m0, s38, 0x2000
	s_add_u32 s38, s8, s57
	global_load_lds_dwordx4 v[194:195], off
	s_addc_u32 s39, s9, s56
	s_mov_b32 m0, s37
	v_mov_b32_e32 v193, v161
	global_load_lds_dwordx4 v160, s[38:39]
	s_mov_b32 m0, s40
	v_lshl_add_u64 v[194:195], s[38:39], 0, v[160:161]
	global_load_lds_dwordx4 v192, s[38:39]
	s_waitcnt vmcnt(8)
	s_waitcnt lgkmcnt(0)
	v_lshl_add_u64 v[192:193], s[38:39], 0, v[192:193]
	s_barrier
	s_setprio 1
	s_nop 1
	s_waitcnt lgkmcnt(0)
	v_mfma_scale_f32_16x16x128_f8f6f4 v[92:95], v[16:23], v[212:219], v[92:95], v199, v198 op_sel_hi:[0,0,0]
	v_mfma_scale_f32_16x16x128_f8f6f4 v[84:87], v[24:31], v[212:219], v[84:87], v199, v198 op_sel_hi:[0,0,0]
	v_mfma_scale_f32_16x16x128_f8f6f4 v[68:71], v[24:31], v[220:227], v[68:71], v199, v198 op_sel_hi:[0,0,0]
	v_mfma_scale_f32_16x16x128_f8f6f4 v[76:79], v[16:23], v[220:227], v[76:79], v199, v198 op_sel_hi:[0,0,0]
	v_mfma_scale_f32_16x16x128_f8f6f4 v[52:55], v[16:23], v[228:235], v[52:55], v199, v198 op_sel_hi:[0,0,0]
	v_mfma_scale_f32_16x16x128_f8f6f4 v[48:51], v[24:31], v[228:235], v[48:51], v199, v198 op_sel_hi:[0,0,0]
	v_mfma_scale_f32_16x16x128_f8f6f4 v[32:35], v[24:31], v[236:243], v[32:35], v199, v198 op_sel_hi:[0,0,0]
	v_mfma_scale_f32_16x16x128_f8f6f4 v[36:39], v[16:23], v[236:243], v[36:39], v199, v198 op_sel_hi:[0,0,0]
	s_setprio 0
	s_setprio 1
	v_mfma_scale_f32_16x16x128_f8f6f4 v[44:47], v[0:7], v[236:243], v[44:47], v199, v198 op_sel_hi:[0,0,0]
	v_mfma_scale_f32_16x16x128_f8f6f4 v[40:43], v[8:15], v[236:243], v[40:43], v199, v198 op_sel_hi:[0,0,0]
	v_mfma_scale_f32_16x16x128_f8f6f4 v[56:59], v[8:15], v[228:235], v[56:59], v199, v198 op_sel_hi:[0,0,0]
	v_mfma_scale_f32_16x16x128_f8f6f4 v[64:67], v[0:7], v[228:235], v[64:67], v199, v198 op_sel_hi:[0,0,0]
	v_mfma_scale_f32_16x16x128_f8f6f4 v[72:75], v[0:7], v[220:227], v[72:75], v199, v198 op_sel_hi:[0,0,0]
	v_mfma_scale_f32_16x16x128_f8f6f4 v[60:63], v[8:15], v[220:227], v[60:63], v199, v198 op_sel_hi:[0,0,0]
	v_mfma_scale_f32_16x16x128_f8f6f4 v[80:83], v[8:15], v[212:219], v[80:83], v199, v198 op_sel_hi:[0,0,0]
	v_mfma_scale_f32_16x16x128_f8f6f4 v[88:91], v[0:7], v[212:219], v[88:91], v199, v198 op_sel_hi:[0,0,0]
	s_setprio 0
	s_barrier
	s_add_i32 s56, 0, 0x18000
	s_add_i32 s57, 0, 0x1c000
	v_add_u32_e32 v0, s56, v204
	v_add_u32_e32 v20, s57, v204
	ds_read_b128 v[8:11], v0
	ds_read_b128 v[12:15], v0 offset:1024
	ds_read_b128 v[24:27], v0 offset:2048
	ds_read_b128 v[28:31], v0 offset:3072
	ds_read_b128 v[0:3], v20
	ds_read_b128 v[4:7], v20 offset:1024
	ds_read_b128 v[16:19], v20 offset:2048
	ds_read_b128 v[20:23], v20 offset:3072
	s_mov_b32 m0, s41
	ds_read_b128 v[212:215], v206 offset:32768
	ds_read_b128 v[216:219], v206 offset:33792
	ds_read_b128 v[220:223], v206 offset:34816
	ds_read_b128 v[224:227], v206 offset:35840
	ds_read_b128 v[228:231], v206 offset:36864
	ds_read_b128 v[232:235], v206 offset:37888
	ds_read_b128 v[236:239], v206 offset:38912
	ds_read_b128 v[240:243], v206 offset:39936
	global_load_lds_dwordx4 v175, s[38:39]
	s_mov_b32 m0, s42
	s_nop 0
	global_load_lds_dwordx4 v177, s[38:39]
	s_waitcnt vmcnt(8)
	s_waitcnt lgkmcnt(0)
	s_barrier
	s_setprio 1
	s_nop 1
	s_waitcnt lgkmcnt(0)
	v_mfma_scale_f32_16x16x128_f8f6f4 v[156:159], v[8:15], v[212:219], v[156:159], v199, v198 op_sel_hi:[0,0,0]
	v_mfma_scale_f32_16x16x128_f8f6f4 v[148:151], v[24:31], v[212:219], v[148:151], v199, v198 op_sel_hi:[0,0,0]
	v_mfma_scale_f32_16x16x128_f8f6f4 v[132:135], v[24:31], v[220:227], v[132:135], v199, v198 op_sel_hi:[0,0,0]
	v_mfma_scale_f32_16x16x128_f8f6f4 v[140:143], v[8:15], v[220:227], v[140:143], v199, v198 op_sel_hi:[0,0,0]
	v_mfma_scale_f32_16x16x128_f8f6f4 v[124:127], v[8:15], v[228:235], v[124:127], v199, v198 op_sel_hi:[0,0,0]
	v_mfma_scale_f32_16x16x128_f8f6f4 v[116:119], v[24:31], v[228:235], v[116:119], v199, v198 op_sel_hi:[0,0,0]
	v_mfma_scale_f32_16x16x128_f8f6f4 v[100:103], v[24:31], v[236:243], v[100:103], v199, v198 op_sel_hi:[0,0,0]
	v_mfma_scale_f32_16x16x128_f8f6f4 v[108:111], v[8:15], v[236:243], v[108:111], v199, v198 op_sel_hi:[0,0,0]
	s_setprio 0
	s_setprio 1
	v_mfma_scale_f32_16x16x128_f8f6f4 v[104:107], v[0:7], v[236:243], v[104:107], v199, v198 op_sel_hi:[0,0,0]
	v_mfma_scale_f32_16x16x128_f8f6f4 v[96:99], v[16:23], v[236:243], v[96:99], v199, v198 op_sel_hi:[0,0,0]
	v_mfma_scale_f32_16x16x128_f8f6f4 v[112:115], v[16:23], v[228:235], v[112:115], v199, v198 op_sel_hi:[0,0,0]
	v_mfma_scale_f32_16x16x128_f8f6f4 v[120:123], v[0:7], v[228:235], v[120:123], v199, v198 op_sel_hi:[0,0,0]
	v_mfma_scale_f32_16x16x128_f8f6f4 v[136:139], v[0:7], v[220:227], v[136:139], v199, v198 op_sel_hi:[0,0,0]
	v_mfma_scale_f32_16x16x128_f8f6f4 v[128:131], v[16:23], v[220:227], v[128:131], v199, v198 op_sel_hi:[0,0,0]
	v_mfma_scale_f32_16x16x128_f8f6f4 v[144:147], v[16:23], v[212:219], v[144:147], v199, v198 op_sel_hi:[0,0,0]
	v_mfma_scale_f32_16x16x128_f8f6f4 v[152:155], v[0:7], v[212:219], v[152:155], v199, v198 op_sel_hi:[0,0,0]
	s_setprio 0
	s_barrier
	s_add_i32 s38, s56, s3
	v_lshl_add_u64 v[188:189], v[188:189], 0, s[22:23]
	s_mov_b32 m0, s38
	ds_read_b128 v[212:215], v206 offset:49152
	ds_read_b128 v[216:219], v206 offset:50176
	ds_read_b128 v[220:223], v206 offset:51200
	ds_read_b128 v[224:227], v206 offset:52224
	ds_read_b128 v[228:231], v206 offset:53248
	ds_read_b128 v[232:235], v206 offset:54272
	ds_read_b128 v[236:239], v206 offset:55296
	ds_read_b128 v[240:243], v206 offset:56320
	global_load_lds_dwordx4 v[188:189], off
	v_lshl_add_u64 v[188:189], v[190:191], 0, s[22:23]
	s_add_i32 m0, s38, 0x2000
	v_lshl_add_u64 v[186:187], v[186:187], 0, s[26:27]
	s_add_i32 s38, s57, s3
	global_load_lds_dwordx4 v[188:189], off
	v_lshl_add_u64 v[188:189], v[186:187], 0, v[164:165]
	s_mov_b32 m0, s38
	v_lshl_add_u64 v[186:187], v[186:187], 0, v[162:163]
	global_load_lds_dwordx4 v[188:189], off
	s_add_i32 m0, s38, 0x2000
	s_nop 0
	global_load_lds_dwordx4 v[186:187], off
	v_lshl_add_u64 v[186:187], v[194:195], 0, s[22:23]
	s_mov_b32 m0, s45
	s_nop 0
	global_load_lds_dwordx4 v[186:187], off
	v_lshl_add_u64 v[186:187], v[192:193], 0, s[22:23]
	s_mov_b32 m0, s46
	s_nop 0
	global_load_lds_dwordx4 v[186:187], off
	s_waitcnt vmcnt(8)
	s_waitcnt lgkmcnt(0)
	s_barrier
	s_setprio 1
	s_nop 1
	s_waitcnt lgkmcnt(0)
	v_mfma_scale_f32_16x16x128_f8f6f4 v[92:95], v[8:15], v[212:219], v[92:95], v199, v198 op_sel_hi:[0,0,0]
	v_mfma_scale_f32_16x16x128_f8f6f4 v[84:87], v[24:31], v[212:219], v[84:87], v199, v198 op_sel_hi:[0,0,0]
	v_mfma_scale_f32_16x16x128_f8f6f4 v[68:71], v[24:31], v[220:227], v[68:71], v199, v198 op_sel_hi:[0,0,0]
	v_mfma_scale_f32_16x16x128_f8f6f4 v[76:79], v[8:15], v[220:227], v[76:79], v199, v198 op_sel_hi:[0,0,0]
	v_mfma_scale_f32_16x16x128_f8f6f4 v[52:55], v[8:15], v[228:235], v[52:55], v199, v198 op_sel_hi:[0,0,0]
	v_mfma_scale_f32_16x16x128_f8f6f4 v[48:51], v[24:31], v[228:235], v[48:51], v199, v198 op_sel_hi:[0,0,0]
	v_mfma_scale_f32_16x16x128_f8f6f4 v[32:35], v[24:31], v[236:243], v[32:35], v199, v198 op_sel_hi:[0,0,0]
	v_mfma_scale_f32_16x16x128_f8f6f4 v[36:39], v[8:15], v[236:243], v[36:39], v199, v198 op_sel_hi:[0,0,0]
	s_setprio 0
	s_setprio 1
	v_mfma_scale_f32_16x16x128_f8f6f4 v[44:47], v[0:7], v[236:243], v[44:47], v199, v198 op_sel_hi:[0,0,0]
	v_mfma_scale_f32_16x16x128_f8f6f4 v[40:43], v[16:23], v[236:243], v[40:43], v199, v198 op_sel_hi:[0,0,0]
	v_mfma_scale_f32_16x16x128_f8f6f4 v[56:59], v[16:23], v[228:235], v[56:59], v199, v198 op_sel_hi:[0,0,0]
	v_mfma_scale_f32_16x16x128_f8f6f4 v[64:67], v[0:7], v[228:235], v[64:67], v199, v198 op_sel_hi:[0,0,0]
	v_mfma_scale_f32_16x16x128_f8f6f4 v[72:75], v[0:7], v[220:227], v[72:75], v199, v198 op_sel_hi:[0,0,0]
	v_mfma_scale_f32_16x16x128_f8f6f4 v[60:63], v[16:23], v[220:227], v[60:63], v199, v198 op_sel_hi:[0,0,0]
	v_mfma_scale_f32_16x16x128_f8f6f4 v[80:83], v[16:23], v[212:219], v[80:83], v199, v198 op_sel_hi:[0,0,0]
	v_mfma_scale_f32_16x16x128_f8f6f4 v[88:91], v[0:7], v[212:219], v[88:91], v199, v198 op_sel_hi:[0,0,0]
	s_setprio 0
	s_barrier
	s_add_i32 s35, s35, 2
	s_cmp_gt_u32 s35, 13
	s_mov_b64 s[38:39], s[6:7]
	s_cbranch_scc0 .LBB0_1149
	s_nop 15
	s_nop 15
	s_and_b64 vcc, exec, s[28:29]
	s_cbranch_vccz .LBB0_1152
	s_barrier

.LBB0_1231:
	s_add_u32 s4, s34, 0x100
	s_addc_u32 s5, s35, 0
	s_cmpk_eq_i32 s34, 0x700
	v_lshl_add_u64 v[0:1], v[184:185], 0, s[34:35]
	s_cselect_b64 vcc, -1, 0
	v_cndmask_b32_e32 v186, v0, v170, vcc
	v_add_u32_e32 v0, s45, v200
	v_add_u32_e32 v12, s46, v200
	v_cndmask_b32_e32 v187, v1, v171, vcc
	ds_read_b128 v[16:19], v0
	ds_read_b128 v[20:23], v0 offset:1024
	ds_read_b128 v[24:27], v0 offset:2048
	ds_read_b128 v[28:31], v0 offset:3072
	ds_read_b128 v[0:3], v12
	ds_read_b128 v[4:7], v12 offset:1024
	ds_read_b128 v[8:11], v12 offset:2048
	ds_read_b128 v[12:15], v12 offset:3072
	s_and_b64 s[50:51], vcc, exec
	v_cndmask_b32_e32 v164, v173, v214, vcc
	v_cndmask_b32_e32 v192, v174, v215, vcc
	v_cndmask_b32_e32 v169, v176, v216, vcc
	v_cndmask_b32_e32 v177, v178, v217, vcc
	s_cselect_b32 s49, 0, s5
	s_cselect_b32 s50, 0, s4
	v_lshl_add_u64 v[188:189], v[182:183], 0, s[34:35]
	s_add_i32 m0, s31, 0xc000
	ds_read_b128 v[218:221], v211
	ds_read_b128 v[222:225], v211 offset:1024
	ds_read_b128 v[226:229], v211 offset:2048
	ds_read_b128 v[230:233], v211 offset:3072
	ds_read_b128 v[234:237], v211 offset:4096
	ds_read_b128 v[238:241], v211 offset:5120
	ds_read_b128 v[242:245], v211 offset:6144
	ds_read_b128 v[246:249], v211 offset:7168
	global_load_lds_dwordx4 v[188:189], off
	v_lshl_add_u64 v[188:189], v[180:181], 0, s[34:35]
	s_add_i32 m0, s31, 0xe000
	s_nop 0
	global_load_lds_dwordx4 v[188:189], off
	s_waitcnt vmcnt(8)
	s_waitcnt lgkmcnt(0)
	s_barrier
	s_setprio 1
	s_nop 1
	s_waitcnt lgkmcnt(0)
	v_mfma_scale_f32_16x16x128_f8f6f4 v[156:159], v[16:23], v[218:225], v[156:159], v197, v196 op_sel_hi:[0,0,0]
	v_mfma_scale_f32_16x16x128_f8f6f4 v[152:155], v[24:31], v[218:225], v[152:155], v197, v196 op_sel_hi:[0,0,0]
	v_mfma_scale_f32_16x16x128_f8f6f4 v[136:139], v[24:31], v[226:233], v[136:139], v197, v196 op_sel_hi:[0,0,0]
	v_mfma_scale_f32_16x16x128_f8f6f4 v[140:143], v[16:23], v[226:233], v[140:143], v197, v196 op_sel_hi:[0,0,0]
	v_mfma_scale_f32_16x16x128_f8f6f4 v[124:127], v[16:23], v[234:241], v[124:127], v197, v196 op_sel_hi:[0,0,0]
	v_mfma_scale_f32_16x16x128_f8f6f4 v[120:123], v[24:31], v[234:241], v[120:123], v197, v196 op_sel_hi:[0,0,0]
	v_mfma_scale_f32_16x16x128_f8f6f4 v[104:107], v[24:31], v[242:249], v[104:107], v197, v196 op_sel_hi:[0,0,0]
	v_mfma_scale_f32_16x16x128_f8f6f4 v[108:111], v[16:23], v[242:249], v[108:111], v197, v196 op_sel_hi:[0,0,0]
	s_setprio 0
	s_setprio 1
	v_mfma_scale_f32_16x16x128_f8f6f4 v[100:103], v[0:7], v[242:249], v[100:103], v197, v196 op_sel_hi:[0,0,0]
	v_mfma_scale_f32_16x16x128_f8f6f4 v[96:99], v[8:15], v[242:249], v[96:99], v197, v196 op_sel_hi:[0,0,0]
	v_mfma_scale_f32_16x16x128_f8f6f4 v[112:115], v[8:15], v[234:241], v[112:115], v197, v196 op_sel_hi:[0,0,0]
	v_mfma_scale_f32_16x16x128_f8f6f4 v[116:119], v[0:7], v[234:241], v[116:119], v197, v196 op_sel_hi:[0,0,0]
	v_mfma_scale_f32_16x16x128_f8f6f4 v[132:135], v[0:7], v[226:233], v[132:135], v197, v196 op_sel_hi:[0,0,0]
	v_mfma_scale_f32_16x16x128_f8f6f4 v[128:131], v[8:15], v[226:233], v[128:131], v197, v196 op_sel_hi:[0,0,0]
	v_mfma_scale_f32_16x16x128_f8f6f4 v[144:147], v[8:15], v[218:225], v[144:147], v197, v196 op_sel_hi:[0,0,0]
	v_mfma_scale_f32_16x16x128_f8f6f4 v[148:151], v[0:7], v[218:225], v[148:151], v197, v196 op_sel_hi:[0,0,0]
	s_setprio 0
	s_barrier
	s_add_i32 s34, s45, s36
	v_lshl_add_u64 v[188:189], v[186:187], 0, v[162:163]
	s_mov_b32 m0, s34
	ds_read_b128 v[218:221], v211 offset:16384
	ds_read_b128 v[222:225], v211 offset:17408
	ds_read_b128 v[226:229], v211 offset:18432
	ds_read_b128 v[230:233], v211 offset:19456
	ds_read_b128 v[234:237], v211 offset:20480
	ds_read_b128 v[238:241], v211 offset:21504
	ds_read_b128 v[242:245], v211 offset:22528
	ds_read_b128 v[246:249], v211 offset:23552
	global_load_lds_dwordx4 v[188:189], off
	v_lshl_add_u64 v[190:191], v[186:187], 0, v[160:161]
	s_add_i32 m0, s34, 0x2000
	v_lshl_add_u64 v[194:195], v[186:187], 0, s[10:11]
	s_add_i32 s34, s46, s36
	global_load_lds_dwordx4 v[190:191], off
	v_lshl_add_u64 v[250:251], v[194:195], 0, v[162:163]
	s_mov_b32 m0, s34
	v_lshl_add_u64 v[194:195], v[194:195], 0, v[160:161]
	global_load_lds_dwordx4 v[250:251], off
	s_add_i32 m0, s34, 0x2000
	s_add_u32 s34, s6, s50
	global_load_lds_dwordx4 v[194:195], off
	s_addc_u32 s35, s7, s49
	s_mov_b32 m0, s31
	v_mov_b32_e32 v193, v165
	global_load_lds_dwordx4 v164, s[34:35]
	s_mov_b32 m0, s38
	v_lshl_add_u64 v[194:195], s[34:35], 0, v[164:165]
	global_load_lds_dwordx4 v192, s[34:35]
	s_waitcnt vmcnt(8)
	s_waitcnt lgkmcnt(0)
	v_lshl_add_u64 v[192:193], s[34:35], 0, v[192:193]
	s_barrier
	s_setprio 1
	s_nop 1
	s_waitcnt lgkmcnt(0)
	v_mfma_scale_f32_16x16x128_f8f6f4 v[92:95], v[16:23], v[218:225], v[92:95], v197, v196 op_sel_hi:[0,0,0]
	v_mfma_scale_f32_16x16x128_f8f6f4 v[88:91], v[24:31], v[218:225], v[88:91], v197, v196 op_sel_hi:[0,0,0]
	v_mfma_scale_f32_16x16x128_f8f6f4 v[72:75], v[24:31], v[226:233], v[72:75], v197, v196 op_sel_hi:[0,0,0]
	v_mfma_scale_f32_16x16x128_f8f6f4 v[76:79], v[16:23], v[226:233], v[76:79], v197, v196 op_sel_hi:[0,0,0]
	v_mfma_scale_f32_16x16x128_f8f6f4 v[52:55], v[16:23], v[234:241], v[52:55], v197, v196 op_sel_hi:[0,0,0]
	v_mfma_scale_f32_16x16x128_f8f6f4 v[40:43], v[24:31], v[234:241], v[40:43], v197, v196 op_sel_hi:[0,0,0]
	v_mfma_scale_f32_16x16x128_f8f6f4 v[32:35], v[24:31], v[242:249], v[32:35], v197, v196 op_sel_hi:[0,0,0]
	v_mfma_scale_f32_16x16x128_f8f6f4 v[36:39], v[16:23], v[242:249], v[36:39], v197, v196 op_sel_hi:[0,0,0]
	s_setprio 0
	s_setprio 1
	v_mfma_scale_f32_16x16x128_f8f6f4 v[44:47], v[0:7], v[242:249], v[44:47], v197, v196 op_sel_hi:[0,0,0]
	v_mfma_scale_f32_16x16x128_f8f6f4 v[48:51], v[8:15], v[242:249], v[48:51], v197, v196 op_sel_hi:[0,0,0]
	v_mfma_scale_f32_16x16x128_f8f6f4 v[68:71], v[8:15], v[234:241], v[68:71], v197, v196 op_sel_hi:[0,0,0]
	v_mfma_scale_f32_16x16x128_f8f6f4 v[64:67], v[0:7], v[234:241], v[64:67], v197, v196 op_sel_hi:[0,0,0]
	v_mfma_scale_f32_16x16x128_f8f6f4 v[60:63], v[0:7], v[226:233], v[60:63], v197, v196 op_sel_hi:[0,0,0]
	v_mfma_scale_f32_16x16x128_f8f6f4 v[56:59], v[8:15], v[226:233], v[56:59], v197, v196 op_sel_hi:[0,0,0]
	v_mfma_scale_f32_16x16x128_f8f6f4 v[80:83], v[8:15], v[218:225], v[80:83], v197, v196 op_sel_hi:[0,0,0]
	v_mfma_scale_f32_16x16x128_f8f6f4 v[84:87], v[0:7], v[218:225], v[84:87], v197, v196 op_sel_hi:[0,0,0]
	s_setprio 0
	s_barrier
	s_add_i32 s49, 0, 0x18000
	s_add_i32 s50, 0, 0x1c000
	v_add_u32_e32 v0, s49, v200
	v_add_u32_e32 v20, s50, v200
	ds_read_b128 v[8:11], v0
	ds_read_b128 v[12:15], v0 offset:1024
	ds_read_b128 v[24:27], v0 offset:2048
	ds_read_b128 v[28:31], v0 offset:3072
	ds_read_b128 v[0:3], v20
	ds_read_b128 v[4:7], v20 offset:1024
	ds_read_b128 v[16:19], v20 offset:2048
	ds_read_b128 v[20:23], v20 offset:3072
	s_mov_b32 m0, s39
	ds_read_b128 v[218:221], v211 offset:32768
	ds_read_b128 v[222:225], v211 offset:33792
	ds_read_b128 v[226:229], v211 offset:34816
	ds_read_b128 v[230:233], v211 offset:35840
	ds_read_b128 v[234:237], v211 offset:36864
	ds_read_b128 v[238:241], v211 offset:37888
	ds_read_b128 v[242:245], v211 offset:38912
	ds_read_b128 v[246:249], v211 offset:39936
	global_load_lds_dwordx4 v169, s[34:35]
	s_mov_b32 m0, s40
	s_nop 0
	global_load_lds_dwordx4 v177, s[34:35]
	s_waitcnt vmcnt(8)
	s_waitcnt lgkmcnt(0)
	s_barrier
	s_setprio 1
	s_nop 1
	s_waitcnt lgkmcnt(0)
	v_mfma_scale_f32_16x16x128_f8f6f4 v[156:159], v[8:15], v[218:225], v[156:159], v197, v196 op_sel_hi:[0,0,0]
	v_mfma_scale_f32_16x16x128_f8f6f4 v[152:155], v[24:31], v[218:225], v[152:155], v197, v196 op_sel_hi:[0,0,0]
	v_mfma_scale_f32_16x16x128_f8f6f4 v[136:139], v[24:31], v[226:233], v[136:139], v197, v196 op_sel_hi:[0,0,0]
	v_mfma_scale_f32_16x16x128_f8f6f4 v[140:143], v[8:15], v[226:233], v[140:143], v197, v196 op_sel_hi:[0,0,0]
	v_mfma_scale_f32_16x16x128_f8f6f4 v[124:127], v[8:15], v[234:241], v[124:127], v197, v196 op_sel_hi:[0,0,0]
	v_mfma_scale_f32_16x16x128_f8f6f4 v[120:123], v[24:31], v[234:241], v[120:123], v197, v196 op_sel_hi:[0,0,0]
	v_mfma_scale_f32_16x16x128_f8f6f4 v[104:107], v[24:31], v[242:249], v[104:107], v197, v196 op_sel_hi:[0,0,0]
	v_mfma_scale_f32_16x16x128_f8f6f4 v[108:111], v[8:15], v[242:249], v[108:111], v197, v196 op_sel_hi:[0,0,0]
	s_setprio 0
	s_setprio 1
	v_mfma_scale_f32_16x16x128_f8f6f4 v[100:103], v[0:7], v[242:249], v[100:103], v197, v196 op_sel_hi:[0,0,0]
	v_mfma_scale_f32_16x16x128_f8f6f4 v[96:99], v[16:23], v[242:249], v[96:99], v197, v196 op_sel_hi:[0,0,0]
	v_mfma_scale_f32_16x16x128_f8f6f4 v[112:115], v[16:23], v[234:241], v[112:115], v197, v196 op_sel_hi:[0,0,0]
	v_mfma_scale_f32_16x16x128_f8f6f4 v[116:119], v[0:7], v[234:241], v[116:119], v197, v196 op_sel_hi:[0,0,0]
	v_mfma_scale_f32_16x16x128_f8f6f4 v[132:135], v[0:7], v[226:233], v[132:135], v197, v196 op_sel_hi:[0,0,0]
	v_mfma_scale_f32_16x16x128_f8f6f4 v[128:131], v[16:23], v[226:233], v[128:131], v197, v196 op_sel_hi:[0,0,0]
	v_mfma_scale_f32_16x16x128_f8f6f4 v[144:147], v[16:23], v[218:225], v[144:147], v197, v196 op_sel_hi:[0,0,0]
	v_mfma_scale_f32_16x16x128_f8f6f4 v[148:151], v[0:7], v[218:225], v[148:151], v197, v196 op_sel_hi:[0,0,0]
	s_setprio 0
	s_barrier
	s_add_i32 s34, s49, s36
	v_lshl_add_u64 v[188:189], v[188:189], 0, s[18:19]
	s_mov_b32 m0, s34
	ds_read_b128 v[218:221], v211 offset:49152
	ds_read_b128 v[222:225], v211 offset:50176
	ds_read_b128 v[226:229], v211 offset:51200
	ds_read_b128 v[230:233], v211 offset:52224
	ds_read_b128 v[234:237], v211 offset:53248
	ds_read_b128 v[238:241], v211 offset:54272
	ds_read_b128 v[242:245], v211 offset:55296
	ds_read_b128 v[246:249], v211 offset:56320
	global_load_lds_dwordx4 v[188:189], off
	v_lshl_add_u64 v[188:189], v[190:191], 0, s[18:19]
	s_add_i32 m0, s34, 0x2000
	v_lshl_add_u64 v[186:187], v[186:187], 0, s[22:23]
	s_add_i32 s34, s50, s36
	global_load_lds_dwordx4 v[188:189], off
	v_lshl_add_u64 v[188:189], v[186:187], 0, v[162:163]
	s_mov_b32 m0, s34
	v_lshl_add_u64 v[186:187], v[186:187], 0, v[160:161]
	global_load_lds_dwordx4 v[188:189], off
	s_add_i32 m0, s34, 0x2000
	s_nop 0
	global_load_lds_dwordx4 v[186:187], off
	v_lshl_add_u64 v[186:187], v[194:195], 0, s[18:19]
	s_mov_b32 m0, s42
	s_nop 0
	global_load_lds_dwordx4 v[186:187], off
	v_lshl_add_u64 v[186:187], v[192:193], 0, s[18:19]
	s_mov_b32 m0, s43
	s_nop 0
	global_load_lds_dwordx4 v[186:187], off
	s_waitcnt vmcnt(8)
	s_waitcnt lgkmcnt(0)
	s_barrier
	s_setprio 1
	s_nop 1
	s_waitcnt lgkmcnt(0)
	v_mfma_scale_f32_16x16x128_f8f6f4 v[92:95], v[8:15], v[218:225], v[92:95], v197, v196 op_sel_hi:[0,0,0]
	v_mfma_scale_f32_16x16x128_f8f6f4 v[88:91], v[24:31], v[218:225], v[88:91], v197, v196 op_sel_hi:[0,0,0]
	v_mfma_scale_f32_16x16x128_f8f6f4 v[72:75], v[24:31], v[226:233], v[72:75], v197, v196 op_sel_hi:[0,0,0]
	v_mfma_scale_f32_16x16x128_f8f6f4 v[76:79], v[8:15], v[226:233], v[76:79], v197, v196 op_sel_hi:[0,0,0]
	v_mfma_scale_f32_16x16x128_f8f6f4 v[52:55], v[8:15], v[234:241], v[52:55], v197, v196 op_sel_hi:[0,0,0]
	v_mfma_scale_f32_16x16x128_f8f6f4 v[40:43], v[24:31], v[234:241], v[40:43], v197, v196 op_sel_hi:[0,0,0]
	v_mfma_scale_f32_16x16x128_f8f6f4 v[32:35], v[24:31], v[242:249], v[32:35], v197, v196 op_sel_hi:[0,0,0]
	v_mfma_scale_f32_16x16x128_f8f6f4 v[36:39], v[8:15], v[242:249], v[36:39], v197, v196 op_sel_hi:[0,0,0]
	s_setprio 0
	s_setprio 1
	v_mfma_scale_f32_16x16x128_f8f6f4 v[44:47], v[0:7], v[242:249], v[44:47], v197, v196 op_sel_hi:[0,0,0]
	v_mfma_scale_f32_16x16x128_f8f6f4 v[48:51], v[16:23], v[242:249], v[48:51], v197, v196 op_sel_hi:[0,0,0]
	v_mfma_scale_f32_16x16x128_f8f6f4 v[68:71], v[16:23], v[234:241], v[68:71], v197, v196 op_sel_hi:[0,0,0]
	v_mfma_scale_f32_16x16x128_f8f6f4 v[64:67], v[0:7], v[234:241], v[64:67], v197, v196 op_sel_hi:[0,0,0]
	v_mfma_scale_f32_16x16x128_f8f6f4 v[60:63], v[0:7], v[226:233], v[60:63], v197, v196 op_sel_hi:[0,0,0]
	v_mfma_scale_f32_16x16x128_f8f6f4 v[56:59], v[16:23], v[226:233], v[56:59], v197, v196 op_sel_hi:[0,0,0]
	v_mfma_scale_f32_16x16x128_f8f6f4 v[80:83], v[16:23], v[218:225], v[80:83], v197, v196 op_sel_hi:[0,0,0]
	v_mfma_scale_f32_16x16x128_f8f6f4 v[84:87], v[0:7], v[218:225], v[84:87], v197, v196 op_sel_hi:[0,0,0]
	s_setprio 0
	s_barrier
	s_add_i32 s29, s29, 2
	s_cmp_gt_u32 s29, 13
	s_mov_b64 s[34:35], s[4:5]
	s_cbranch_scc0 .LBB0_1231
	s_nop 15
	s_nop 15
	s_and_b64 vcc, exec, s[24:25]
	s_cbranch_vccz .LBB0_1234
	s_barrier
